# combine phase: loads of both tokens of each unrolled pair issued together (second token prefetched into fresh registers)
# speedup vs baseline: 1.0069x; 1.0069x over previous
; #define YB WSP(unsigned char, W_YB)
; __device__ __forceinline__ void combine_phase(LAS unsigned char* lds, const bf16_t* X, bf16_t* Xo, const unsigned char* __restrict__ YB, const float* __restrict__ mod_l, const int* __restrict__ cnt_l, ...
;     ...
;         for (int i = 0; i < 8; ++i) {
;             const int t = t0 + i;
;             u32x4 yv[4];
; #pragma unroll
;             for (int k = 0; k < 4; ++k) { const int row = __builtin_amdgcn_readlane(rowv, i * 4 + k); yv[k] = __builtin_nontemporal_load((const u32x4*)(YB + (size_t)row * D + k0)); }
;             const u32x4 x0 = *(const u32x4*)(X + (size_t)t * D + k0), x1 = *(const u32x4*)(X + (size_t)t * D + k0 + 8);
;             f32x4 v[4]; float ss = 0.f;
; #pragma unroll
;             for (int q = 0; q < 4; ++q) {
;                 f32x4 a = (f32x4){0.f, 0.f, 0.f, 0.f};
; #pragma unroll
;                 for (int k = 0; k < 4; ++k) { const unsigned w = q == 0 ? yv[k].x : q == 1 ? yv[k].y : q == 2 ? yv[k].z : yv[k].w;
;                     const f32x2_t lo = __builtin_amdgcn_cvt_pk_f32_fp8((int)w, false), hi = __builtin_amdgcn_cvt_pk_f32_fp8((int)w, true);
;                     a[0] += lo.x; a[1] += lo.y; a[2] += hi.x; a[3] += hi.y; }
;                 const u32x4 xq = (q >> 1) ? x1 : x0; const unsigned xa = (q & 1) ? xq.z : xq.x, xb = (q & 1) ? xq.w : xq.y;
;                 v[q] = (f32x4){__uint_as_float(xa << 16), __uint_as_float(xa & 0xffff0000u), __uint_as_float(xb << 16), __uint_as_float(xb & 0xffff0000u)} + g2[q] * a;
;                 ss += v[q][0] * v[q][0] + v[q][1] * v[q][1] + v[q][2] * v[q][2] + v[q][3] * v[q][3];
;             }
.LBB0_1508:
	s_add_i32 s18, s21, -7
	v_readlane_b32 s18, v109, s18
	s_ashr_i32 s19, s18, 31
	s_lshl_b64 s[18:19], s[18:19], 10
	v_lshl_add_u64 v[52:53], v[72:73], 0, s[18:19]
	s_add_i32 s18, s21, -6
	v_readlane_b32 s18, v109, s18
	s_ashr_i32 s19, s18, 31
	s_lshl_b64 s[18:19], s[18:19], 10
	v_lshl_add_u64 v[56:57], v[72:73], 0, s[18:19]
	s_add_i32 s18, s21, -5
	v_readlane_b32 s18, v109, s18
	s_ashr_i32 s19, s18, 31
	s_lshl_b64 s[18:19], s[18:19], 10
	v_lshl_add_u64 v[60:61], v[72:73], 0, s[18:19]
	s_add_i32 s18, s21, -4
	v_readlane_b32 s18, v109, s18
	global_load_dwordx4 v[52:55], v[52:53], off nt
	s_ashr_i32 s19, s18, 31
	global_load_dwordx4 v[56:59], v[56:57], off nt
	s_lshl_b64 s[18:19], s[18:19], 10
	global_load_dwordx4 v[60:63], v[60:61], off nt
	v_lshl_add_u64 v[64:65], v[72:73], 0, s[18:19]
	global_load_dwordx4 v[64:67], v[64:65], off nt
	v_ashrrev_i32_e32 v99, 31, v98
	v_lshlrev_b64 v[68:69], 11, v[98:99]
	v_lshl_add_u64 v[102:103], v[74:75], 0, v[68:69]
	global_load_dwordx4 v[68:71], v[102:103], off offset:16
	global_load_dwordx4 v[110:113], v[102:103], off
	s_add_i32 s18, s21, -3
	v_readlane_b32 s18, v109, s18
	s_ashr_i32 s19, s18, 31
	s_lshl_b64 s[18:19], s[18:19], 10
	v_lshl_add_u64 v[182:183], v[72:73], 0, s[18:19]
	global_load_dwordx4 v[182:185], v[182:183], off nt
	s_add_i32 s18, s21, -2
	v_readlane_b32 s18, v109, s18
	s_ashr_i32 s19, s18, 31
	s_lshl_b64 s[18:19], s[18:19], 10
	v_lshl_add_u64 v[186:187], v[72:73], 0, s[18:19]
	global_load_dwordx4 v[186:189], v[186:187], off nt
	s_add_i32 s18, s21, -1
	v_readlane_b32 s18, v109, s18
	s_ashr_i32 s19, s18, 31
	s_lshl_b64 s[18:19], s[18:19], 10
	v_lshl_add_u64 v[190:191], v[72:73], 0, s[18:19]
	global_load_dwordx4 v[190:193], v[190:191], off nt
	v_readlane_b32 s18, v109, s21
	s_ashr_i32 s19, s18, 31
	s_lshl_b64 s[18:19], s[18:19], 10
	v_lshl_add_u64 v[194:195], v[72:73], 0, s[18:19]
	global_load_dwordx4 v[194:197], v[194:195], off nt
	v_add_u32_e32 v208, 1, v98
	v_ashrrev_i32_e32 v209, 31, v208
	v_lshlrev_b64 v[208:209], 11, v[208:209]
	v_lshl_add_u64 v[206:207], v[74:75], 0, v[208:209]
	global_load_dwordx4 v[198:201], v[206:207], off offset:16
	global_load_dwordx4 v[202:205], v[206:207], off
	s_mov_b32 s18, 0x358637bd
	v_lshlrev_b64 v[100:101], 10, v[98:99]
	s_waitcnt vmcnt(11)
	v_cvt_pk_f32_fp8_e32 v[102:103], v52
	v_cvt_pk_f32_fp8_sdwa v[104:105], v52 src0_sel:WORD_1
	s_waitcnt vmcnt(10)
	v_cvt_pk_f32_fp8_e32 v[114:115], v56
	v_cvt_pk_f32_fp8_sdwa v[116:117], v56 src0_sel:WORD_1
	s_waitcnt vmcnt(9)
	v_cvt_pk_f32_fp8_e32 v[118:119], v60
	v_cvt_pk_f32_fp8_sdwa v[120:121], v60 src0_sel:WORD_1
	s_waitcnt vmcnt(8)
	v_cvt_pk_f32_fp8_e32 v[122:123], v64
	v_cvt_pk_f32_fp8_sdwa v[124:125], v64 src0_sel:WORD_1
	v_pk_add_f32 v[104:105], v[104:105], 0 op_sel_hi:[1,0]
	v_pk_add_f32 v[102:103], v[102:103], 0 op_sel_hi:[1,0]
	v_pk_add_f32 v[104:105], v[104:105], v[116:117]
	v_pk_add_f32 v[102:103], v[102:103], v[114:115]
	v_pk_add_f32 v[104:105], v[104:105], v[120:121]
	v_pk_add_f32 v[102:103], v[102:103], v[118:119]
	v_cvt_pk_f32_fp8_e32 v[116:117], v61
	v_pk_add_f32 v[114:115], v[102:103], v[122:123]
	v_pk_add_f32 v[102:103], v[104:105], v[124:125]
	s_waitcnt vmcnt(6)
	v_lshlrev_b32_e32 v104, 16, v110
	v_and_b32_e32 v105, 0xffff0000, v110
	v_lshlrev_b32_e32 v110, 16, v111
	v_and_b32_e32 v111, 0xffff0000, v111
	v_pk_fma_f32 v[102:103], v[94:95], v[102:103], v[110:111]
	v_cvt_pk_f32_fp8_e32 v[110:111], v53
	v_pk_fma_f32 v[104:105], v[96:97], v[114:115], v[104:105]
	v_cvt_pk_f32_fp8_sdwa v[52:53], v53 src0_sel:WORD_1
	v_cvt_pk_f32_fp8_e32 v[114:115], v57
	v_cvt_pk_f32_fp8_sdwa v[56:57], v57 src0_sel:WORD_1
	v_cvt_pk_f32_fp8_sdwa v[60:61], v61 src0_sel:WORD_1
	v_cvt_pk_f32_fp8_e32 v[118:119], v65
	v_cvt_pk_f32_fp8_sdwa v[64:65], v65 src0_sel:WORD_1
	v_pk_add_f32 v[110:111], v[110:111], 0 op_sel_hi:[1,0]
	v_pk_add_f32 v[52:53], v[52:53], 0 op_sel_hi:[1,0]
	v_pk_add_f32 v[110:111], v[110:111], v[114:115]
	v_pk_add_f32 v[52:53], v[52:53], v[56:57]
	v_pk_add_f32 v[56:57], v[110:111], v[116:117]
	v_pk_add_f32 v[52:53], v[52:53], v[60:61]
	v_pk_add_f32 v[56:57], v[56:57], v[118:119]
	v_lshlrev_b32_e32 v60, 16, v112
	v_and_b32_e32 v61, 0xffff0000, v112
	v_pk_add_f32 v[52:53], v[52:53], v[64:65]
	v_lshlrev_b32_e32 v64, 16, v113
	v_and_b32_e32 v65, 0xffff0000, v113
	v_pk_fma_f32 v[56:57], v[92:93], v[56:57], v[60:61]
	v_pk_fma_f32 v[52:53], v[90:91], v[52:53], v[64:65]
	v_mov_b32_e32 v64, v105
	v_mov_b32_e32 v65, v57
	v_mov_b32_e32 v60, v104
	v_mov_b32_e32 v61, v56
	v_pk_mul_f32 v[64:65], v[64:65], v[64:65]
	v_cvt_pk_f32_fp8_sdwa v[110:111], v54 src0_sel:WORD_1
	v_pk_fma_f32 v[60:61], v[60:61], v[60:61], v[64:65]
	v_mov_b32_e32 v64, v102
	v_mov_b32_e32 v65, v52
	v_pk_fma_f32 v[60:61], v[64:65], v[64:65], v[60:61]
	v_mov_b32_e32 v64, v103
	v_mov_b32_e32 v65, v53
	v_pk_fma_f32 v[60:61], v[64:65], v[64:65], v[60:61]
	v_cvt_pk_f32_fp8_e32 v[64:65], v54
	v_cvt_pk_f32_fp8_e32 v[112:113], v58
	v_cvt_pk_f32_fp8_sdwa v[114:115], v58 src0_sel:WORD_1
	v_cvt_pk_f32_fp8_e32 v[116:117], v62
	v_cvt_pk_f32_fp8_sdwa v[118:119], v62 src0_sel:WORD_1
	v_cvt_pk_f32_fp8_e32 v[120:121], v66
	v_cvt_pk_f32_fp8_sdwa v[122:123], v66 src0_sel:WORD_1
	v_pk_add_f32 v[110:111], v[110:111], 0 op_sel_hi:[1,0]
	v_pk_add_f32 v[64:65], v[64:65], 0 op_sel_hi:[1,0]
	v_pk_add_f32 v[110:111], v[110:111], v[114:115]
	v_pk_add_f32 v[64:65], v[64:65], v[112:113]
; __device__ __forceinline__ void combine_phase(LAS unsigned char* lds, const bf16_t* X, bf16_t* Xo, const unsigned char* __restrict__ YB, const float* __restrict__ mod_l, const int* __restrict__ cnt_l, ...
;     ...
;             for (int q = 0; q < 4; ++q) {
;                 f32x4 a = (f32x4){0.f, 0.f, 0.f, 0.f};
; #pragma unroll
;                 for (int k = 0; k < 4; ++k) { const unsigned w = q == 0 ? yv[k].x : q == 1 ? yv[k].y : q == 2 ? yv[k].z : yv[k].w;
;                     const f32x2_t lo = __builtin_amdgcn_cvt_pk_f32_fp8((int)w, false), hi = __builtin_amdgcn_cvt_pk_f32_fp8((int)w, true);
;                     a[0] += lo.x; a[1] += lo.y; a[2] += hi.x; a[3] += hi.y; }
;                 const u32x4 xq = (q >> 1) ? x1 : x0; const unsigned xa = (q & 1) ? xq.z : xq.x, xb = (q & 1) ? xq.w : xq.y;
;                 v[q] = (f32x4){__uint_as_float(xa << 16), __uint_as_float(xa & 0xffff0000u), __uint_as_float(xb << 16), __uint_as_float(xb & 0xffff0000u)} + g2[q] * a;
;                 ss += v[q][0] * v[q][0] + v[q][1] * v[q][1] + v[q][2] * v[q][2] + v[q][3] * v[q][3];
;             }
;             for (int of = 32; of > 0; of >>= 1) ss += shx(ss, of);
;             const float r = rsqrtf(ss * (1.f / D) + kf(EPS));
;             if (mod_n) {
;                 u32x4 xo0, xo1, h0, h1;
;                 xo0.x = cvt_pk_bf16(v[0][0], v[0][1]); xo0.y = cvt_pk_bf16(v[0][2], v[0][3]); xo0.z = cvt_pk_bf16(v[1][0], v[1][1]); xo0.w = cvt_pk_bf16(v[1][2], v[1][3]);
;                 xo1.x = cvt_pk_bf16(v[2][0], v[2][1]); xo1.y = cvt_pk_bf16(v[2][2], v[2][3]); xo1.z = cvt_pk_bf16(v[3][0], v[3][1]); xo1.w = cvt_pk_bf16(v[3][2], v[3][3]);
;                 *(u32x4*)(Xo + (size_t)t * D + k0) = xo0; *(u32x4*)(Xo + (size_t)t * D + k0 + 8) = xo1;
;                 f32x4 o[4];
; #pragma unroll
;                 for (int q = 0; q < 4; ++q) o[q] = v[q] * r * gn[q] + sh[q];
;                 h0.x = cvt_pk_bf16(o[0][0], o[0][1]); h0.y = cvt_pk_bf16(o[0][2], o[0][3]); h0.z = cvt_pk_bf16(o[1][0], o[1][1]); h0.w = cvt_pk_bf16(o[1][2], o[1][3]);
;                 h1.x = cvt_pk_bf16(o[2][0], o[2][1]); h1.y = cvt_pk_bf16(o[2][2], o[2][3]); h1.z = cvt_pk_bf16(o[3][0], o[3][1]); h1.w = cvt_pk_bf16(o[3][2], o[3][3]);
;                 *(u32x4*)(H1B + (size_t)t * D + k0) = h0; *(u32x4*)(H1B + (size_t)t * D + k0 + 8) = h1;
	v_pk_add_f32 v[110:111], v[110:111], v[118:119]
	v_pk_add_f32 v[64:65], v[64:65], v[116:117]
	v_cvt_pk_f32_fp8_e32 v[114:115], v63
	v_pk_add_f32 v[112:113], v[64:65], v[120:121]
	v_pk_add_f32 v[64:65], v[110:111], v[122:123]
	v_lshlrev_b32_e32 v110, 16, v68
	v_and_b32_e32 v111, 0xffff0000, v68
	v_lshlrev_b32_e32 v68, 16, v69
	v_and_b32_e32 v69, 0xffff0000, v69
	v_pk_fma_f32 v[64:65], v[86:87], v[64:65], v[68:69]
	v_pk_fma_f32 v[68:69], v[88:89], v[112:113], v[110:111]
	v_cvt_pk_f32_fp8_e32 v[110:111], v55
	v_cvt_pk_f32_fp8_sdwa v[54:55], v55 src0_sel:WORD_1
	v_cvt_pk_f32_fp8_e32 v[112:113], v59
	v_cvt_pk_f32_fp8_sdwa v[58:59], v59 src0_sel:WORD_1
	v_cvt_pk_f32_fp8_sdwa v[62:63], v63 src0_sel:WORD_1
	v_cvt_pk_f32_fp8_e32 v[116:117], v67
	v_cvt_pk_f32_fp8_sdwa v[66:67], v67 src0_sel:WORD_1
	v_pk_add_f32 v[110:111], v[110:111], 0 op_sel_hi:[1,0]
	v_pk_add_f32 v[54:55], v[54:55], 0 op_sel_hi:[1,0]
	v_pk_add_f32 v[110:111], v[110:111], v[112:113]
	v_pk_add_f32 v[54:55], v[54:55], v[58:59]
	v_pk_add_f32 v[58:59], v[110:111], v[114:115]
	v_pk_add_f32 v[54:55], v[54:55], v[62:63]
	v_pk_add_f32 v[58:59], v[58:59], v[116:117]
	v_lshlrev_b32_e32 v62, 16, v70
	v_and_b32_e32 v63, 0xffff0000, v70
	v_pk_add_f32 v[54:55], v[54:55], v[66:67]
	v_lshlrev_b32_e32 v66, 16, v71
	v_and_b32_e32 v67, 0xffff0000, v71
	v_pk_fma_f32 v[58:59], v[84:85], v[58:59], v[62:63]
	v_pk_fma_f32 v[54:55], v[82:83], v[54:55], v[66:67]
	v_mov_b32_e32 v66, v69
	v_mov_b32_e32 v67, v59
	v_mov_b32_e32 v62, v68
	v_mov_b32_e32 v63, v58
	v_pk_mul_f32 v[66:67], v[66:67], v[66:67]
	v_add_f32_e32 v60, v60, v61
	v_pk_fma_f32 v[62:63], v[62:63], v[62:63], v[66:67]
	v_mov_b32_e32 v66, v64
	v_mov_b32_e32 v67, v54
	v_pk_fma_f32 v[62:63], v[66:67], v[66:67], v[62:63]
	v_mov_b32_e32 v66, v65
	v_mov_b32_e32 v67, v55
	v_pk_fma_f32 v[62:63], v[66:67], v[66:67], v[62:63]
	v_mbcnt_lo_u32_b32 v61, -1, 0
	v_mbcnt_hi_u32_b32 v61, -1, v61
	s_nop 0
	v_add_f32_e32 v60, v60, v62
	v_lshlrev_b32_e32 v61, 2, v61
	v_add_f32_e32 v60, v60, v63
	v_xor_b32_e32 v61, 0x80, v61
	ds_bpermute_b32 v61, v61, v60
	s_waitcnt lgkmcnt(0)
	v_add_f32_e32 v60, v60, v61
	v_mbcnt_lo_u32_b32 v61, -1, 0
	v_mbcnt_hi_u32_b32 v61, -1, v61
	s_nop 0
	v_lshlrev_b32_e32 v61, 2, v61
	v_xor_b32_e32 v61, 64, v61
	ds_bpermute_b32 v61, v61, v60
	s_waitcnt lgkmcnt(0)
	v_add_f32_e32 v60, v60, v61
	v_mbcnt_lo_u32_b32 v61, -1, 0
	v_mbcnt_hi_u32_b32 v61, -1, v61
	s_nop 0
	v_lshlrev_b32_e32 v61, 2, v61
	v_xor_b32_e32 v61, 32, v61
	ds_bpermute_b32 v61, v61, v60
	s_waitcnt lgkmcnt(0)
	v_add_f32_e32 v60, v60, v61
	v_mbcnt_lo_u32_b32 v61, -1, 0
	v_mbcnt_hi_u32_b32 v61, -1, v61
	s_nop 0
	v_lshlrev_b32_e32 v61, 2, v61
	v_xor_b32_e32 v61, 16, v61
	ds_bpermute_b32 v61, v61, v60
	s_waitcnt lgkmcnt(0)
	v_add_f32_e32 v60, v60, v61
	v_mbcnt_lo_u32_b32 v61, -1, 0
	v_mbcnt_hi_u32_b32 v61, -1, v61
	s_nop 0
	v_lshlrev_b32_e32 v61, 2, v61
	v_xor_b32_e32 v61, 8, v61
	ds_bpermute_b32 v61, v61, v60
	s_waitcnt lgkmcnt(0)
	v_add_f32_e32 v60, v60, v61
	v_mbcnt_lo_u32_b32 v61, -1, 0
	v_mbcnt_hi_u32_b32 v61, -1, v61
	s_nop 0
	v_lshlrev_b32_e32 v61, 2, v61
	v_xor_b32_e32 v61, 4, v61
	ds_bpermute_b32 v61, v61, v60
	s_waitcnt lgkmcnt(0)
	v_add_f32_e32 v60, v60, v61
	v_mov_b32_e32 v61, s18
	v_fmac_f32_e32 v61, 0x3a800000, v60
	v_cmp_gt_f32_e32 vcc, s80, v61
	v_mul_f32_e32 v60, 0x4b800000, v61
	s_nop 0
	v_cndmask_b32_e32 v60, v61, v60, vcc
	v_rsq_f32_e32 v60, v60
	s_nop 0
	v_mul_f32_e32 v61, 0x45800000, v60
	v_cndmask_b32_e32 v60, v60, v61, vcc
	s_and_b64 vcc, exec, s[16:17]
	s_cbranch_vccz .LBB0_1513
	v_lshlrev_b64 v[62:63], 1, v[100:101]
	v_cvt_pk_bf16_f32 v110, v104, v105
	v_cvt_pk_bf16_f32 v111, v102, v103
	v_cvt_pk_bf16_f32 v112, v56, v57
	v_cvt_pk_bf16_f32 v113, v52, v53
	v_lshl_add_u64 v[66:67], v[76:77], 0, v[62:63]
	v_cvt_pk_bf16_f32 v114, v68, v69
	v_cvt_pk_bf16_f32 v115, v64, v65
	v_cvt_pk_bf16_f32 v116, v58, v59
	v_cvt_pk_bf16_f32 v117, v54, v55
	global_store_dwordx4 v[66:67], v[110:113], off
	global_store_dwordx4 v[66:67], v[114:117], off offset:16
	v_pk_mul_f32 v[66:67], v[102:103], v[60:61] op_sel_hi:[1,0]
	v_pk_mul_f32 v[110:111], v[52:53], v[60:61] op_sel_hi:[1,0]
	v_pk_mul_f32 v[70:71], v[104:105], v[60:61] op_sel_hi:[1,0]
	v_pk_mul_f32 v[112:113], v[56:57], v[60:61] op_sel_hi:[1,0]
	v_pk_fma_f32 v[114:115], v[32:33], v[110:111], v[20:21]
	v_pk_mul_f32 v[110:111], v[64:65], v[60:61] op_sel_hi:[1,0]
	v_pk_fma_f32 v[66:67], v[28:29], v[66:67], v[24:25]
	v_pk_fma_f32 v[70:71], v[26:27], v[70:71], v[22:23]
	v_pk_fma_f32 v[112:113], v[30:31], v[112:113], v[18:19]
	v_pk_mul_f32 v[116:117], v[68:69], v[60:61] op_sel_hi:[1,0]
	v_pk_fma_f32 v[118:119], v[46:47], v[110:111], v[42:43]
	v_pk_mul_f32 v[110:111], v[54:55], v[60:61] op_sel_hi:[1,0]
	v_pk_mul_f32 v[120:121], v[58:59], v[60:61] op_sel_hi:[1,0]
	v_pk_fma_f32 v[116:117], v[44:45], v[116:117], v[40:41]
	v_pk_fma_f32 v[122:123], v[50:51], v[110:111], v[38:39]
	v_pk_fma_f32 v[120:121], v[48:49], v[120:121], v[36:37]
	v_cvt_pk_bf16_f32 v110, v70, v71
	v_cvt_pk_bf16_f32 v111, v66, v67
	v_cvt_pk_bf16_f32 v112, v112, v113
	v_cvt_pk_bf16_f32 v113, v114, v115
	v_lshl_add_u64 v[62:63], v[78:79], 0, v[62:63]
	v_cvt_pk_bf16_f32 v114, v116, v117
	v_cvt_pk_bf16_f32 v115, v118, v119
	v_cvt_pk_bf16_f32 v116, v120, v121
	v_cvt_pk_bf16_f32 v117, v122, v123
	global_store_dwordx4 v[62:63], v[110:113], off
	global_store_dwordx4 v[62:63], v[114:117], off offset:16
	s_cbranch_execnz .LBB0_1511

; __device__ __forceinline__ float kf(float x) { asm volatile("" : "+s"(x)); return x; }
; __device__ __forceinline__ float shx(float v, int m) { int ln; asm volatile("v_mbcnt_lo_u32_b32 %0, -1, 0\n\tv_mbcnt_hi_u32_b32 %0, -1, %0" : "=v"(ln)); return __builtin_bit_cast(float, __builtin_amdgcn_ds_bpermute((ln ^ m) << 2, __builtin_bit_cast(int, v))); }
; #define YB WSP(unsigned char, W_YB)
; __device__ __forceinline__ void combine_phase(LAS unsigned char* lds, const bf16_t* X, bf16_t* Xo, const unsigned char* __restrict__ YB, const float* __restrict__ mod_l, const int* __restrict__ cnt_l, ...
;     ...
;         for (int i = 0; i < 8; ++i) {
;             const int t = t0 + i;
;             u32x4 yv[4];
; #pragma unroll
;             for (int k = 0; k < 4; ++k) { const int row = __builtin_amdgcn_readlane(rowv, i * 4 + k); yv[k] = __builtin_nontemporal_load((const u32x4*)(YB + (size_t)row * D + k0)); }
;             const u32x4 x0 = *(const u32x4*)(X + (size_t)t * D + k0), x1 = *(const u32x4*)(X + (size_t)t * D + k0 + 8);
;             f32x4 v[4]; float ss = 0.f;
; #pragma unroll
;             for (int q = 0; q < 4; ++q) {
;                 f32x4 a = (f32x4){0.f, 0.f, 0.f, 0.f};
; #pragma unroll
;                 for (int k = 0; k < 4; ++k) { const unsigned w = q == 0 ? yv[k].x : q == 1 ? yv[k].y : q == 2 ? yv[k].z : yv[k].w;
;                     const f32x2_t lo = __builtin_amdgcn_cvt_pk_f32_fp8((int)w, false), hi = __builtin_amdgcn_cvt_pk_f32_fp8((int)w, true);
;                     a[0] += lo.x; a[1] += lo.y; a[2] += hi.x; a[3] += hi.y; }
;                 const u32x4 xq = (q >> 1) ? x1 : x0; const unsigned xa = (q & 1) ? xq.z : xq.x, xb = (q & 1) ? xq.w : xq.y;
;                 v[q] = (f32x4){__uint_as_float(xa << 16), __uint_as_float(xa & 0xffff0000u), __uint_as_float(xb << 16), __uint_as_float(xb & 0xffff0000u)} + g2[q] * a;
;                 ss += v[q][0] * v[q][0] + v[q][1] * v[q][1] + v[q][2] * v[q][2] + v[q][3] * v[q][3];
;             }
;             for (int of = 32; of > 0; of >>= 1) ss += shx(ss, of);
;             const float r = rsqrtf(ss * (1.f / D) + kf(EPS));
.LBB0_1511:
	v_add_u32_e32 v68, 1, v98
	v_ashrrev_i32_e32 v69, 31, v68
	v_lshlrev_b64 v[100:101], 10, v[68:69]
	s_mov_b32 s18, 0x358637bd
	s_waitcnt vmcnt(9)
	v_cvt_pk_f32_fp8_e32 v[102:103], v182
	v_cvt_pk_f32_fp8_sdwa v[104:105], v182 src0_sel:WORD_1
	s_waitcnt vmcnt(8)
	v_cvt_pk_f32_fp8_e32 v[114:115], v186
	v_cvt_pk_f32_fp8_sdwa v[116:117], v186 src0_sel:WORD_1
	s_waitcnt vmcnt(7)
	v_cvt_pk_f32_fp8_e32 v[118:119], v190
	v_cvt_pk_f32_fp8_sdwa v[120:121], v190 src0_sel:WORD_1
	s_waitcnt vmcnt(6)
	v_cvt_pk_f32_fp8_e32 v[122:123], v194
	v_cvt_pk_f32_fp8_sdwa v[124:125], v194 src0_sel:WORD_1
	v_pk_add_f32 v[104:105], v[104:105], 0 op_sel_hi:[1,0]
	v_pk_add_f32 v[102:103], v[102:103], 0 op_sel_hi:[1,0]
	v_pk_add_f32 v[104:105], v[104:105], v[116:117]
	v_pk_add_f32 v[102:103], v[102:103], v[114:115]
	v_pk_add_f32 v[104:105], v[104:105], v[120:121]
	v_pk_add_f32 v[102:103], v[102:103], v[118:119]
	v_cvt_pk_f32_fp8_e32 v[116:117], v191
	v_pk_add_f32 v[114:115], v[102:103], v[122:123]
	v_pk_add_f32 v[102:103], v[104:105], v[124:125]
	s_waitcnt vmcnt(4)
	v_lshlrev_b32_e32 v104, 16, v202
	v_and_b32_e32 v105, 0xffff0000, v202
	v_lshlrev_b32_e32 v110, 16, v203
	v_and_b32_e32 v111, 0xffff0000, v203
	v_pk_fma_f32 v[102:103], v[94:95], v[102:103], v[110:111]
	v_cvt_pk_f32_fp8_e32 v[110:111], v183
	v_pk_fma_f32 v[104:105], v[96:97], v[114:115], v[104:105]
	v_cvt_pk_f32_fp8_sdwa v[52:53], v183 src0_sel:WORD_1
	v_cvt_pk_f32_fp8_e32 v[114:115], v187
	v_cvt_pk_f32_fp8_sdwa v[56:57], v187 src0_sel:WORD_1
	v_cvt_pk_f32_fp8_sdwa v[60:61], v191 src0_sel:WORD_1
	v_cvt_pk_f32_fp8_e32 v[118:119], v195
	v_cvt_pk_f32_fp8_sdwa v[64:65], v195 src0_sel:WORD_1
	v_pk_add_f32 v[110:111], v[110:111], 0 op_sel_hi:[1,0]
	v_pk_add_f32 v[52:53], v[52:53], 0 op_sel_hi:[1,0]
	v_pk_add_f32 v[110:111], v[110:111], v[114:115]
	v_pk_add_f32 v[52:53], v[52:53], v[56:57]
	v_pk_add_f32 v[56:57], v[110:111], v[116:117]
	v_pk_add_f32 v[52:53], v[52:53], v[60:61]
	v_pk_add_f32 v[56:57], v[56:57], v[118:119]
	v_lshlrev_b32_e32 v60, 16, v204
	v_and_b32_e32 v61, 0xffff0000, v204
	v_pk_add_f32 v[52:53], v[52:53], v[64:65]
	v_lshlrev_b32_e32 v64, 16, v205
	v_and_b32_e32 v65, 0xffff0000, v205
	v_pk_fma_f32 v[56:57], v[92:93], v[56:57], v[60:61]
	v_pk_fma_f32 v[52:53], v[90:91], v[52:53], v[64:65]
	v_mov_b32_e32 v64, v105
	v_mov_b32_e32 v65, v57
	v_mov_b32_e32 v60, v104
	v_mov_b32_e32 v61, v56
	v_pk_mul_f32 v[64:65], v[64:65], v[64:65]
	v_cvt_pk_f32_fp8_sdwa v[110:111], v184 src0_sel:WORD_1
	v_pk_fma_f32 v[60:61], v[60:61], v[60:61], v[64:65]
	v_mov_b32_e32 v64, v102
	v_mov_b32_e32 v65, v52
	v_pk_fma_f32 v[60:61], v[64:65], v[64:65], v[60:61]
	v_mov_b32_e32 v64, v103
	v_mov_b32_e32 v65, v53
	v_pk_fma_f32 v[60:61], v[64:65], v[64:65], v[60:61]
	v_cvt_pk_f32_fp8_e32 v[64:65], v184
	v_cvt_pk_f32_fp8_e32 v[112:113], v188
	v_cvt_pk_f32_fp8_sdwa v[114:115], v188 src0_sel:WORD_1
	v_cvt_pk_f32_fp8_e32 v[116:117], v192
	v_cvt_pk_f32_fp8_sdwa v[118:119], v192 src0_sel:WORD_1
	v_cvt_pk_f32_fp8_e32 v[120:121], v196
	v_cvt_pk_f32_fp8_sdwa v[122:123], v196 src0_sel:WORD_1
	v_pk_add_f32 v[110:111], v[110:111], 0 op_sel_hi:[1,0]
	v_pk_add_f32 v[64:65], v[64:65], 0 op_sel_hi:[1,0]
	v_pk_add_f32 v[110:111], v[110:111], v[114:115]
	v_pk_add_f32 v[64:65], v[64:65], v[112:113]
	v_pk_add_f32 v[110:111], v[110:111], v[118:119]
	v_pk_add_f32 v[64:65], v[64:65], v[116:117]
	v_cvt_pk_f32_fp8_e32 v[114:115], v193
	v_pk_add_f32 v[112:113], v[64:65], v[120:121]
	v_pk_add_f32 v[64:65], v[110:111], v[122:123]
	v_lshlrev_b32_e32 v110, 16, v198
	v_and_b32_e32 v111, 0xffff0000, v198
	v_lshlrev_b32_e32 v68, 16, v199
	v_and_b32_e32 v69, 0xffff0000, v199
	v_pk_fma_f32 v[64:65], v[86:87], v[64:65], v[68:69]
	v_pk_fma_f32 v[68:69], v[88:89], v[112:113], v[110:111]
	v_cvt_pk_f32_fp8_e32 v[110:111], v185
	v_cvt_pk_f32_fp8_sdwa v[54:55], v185 src0_sel:WORD_1
	v_cvt_pk_f32_fp8_e32 v[112:113], v189
	v_cvt_pk_f32_fp8_sdwa v[58:59], v189 src0_sel:WORD_1
	v_cvt_pk_f32_fp8_sdwa v[62:63], v193 src0_sel:WORD_1
	v_cvt_pk_f32_fp8_e32 v[116:117], v197
	v_cvt_pk_f32_fp8_sdwa v[66:67], v197 src0_sel:WORD_1
	v_pk_add_f32 v[110:111], v[110:111], 0 op_sel_hi:[1,0]
	v_pk_add_f32 v[54:55], v[54:55], 0 op_sel_hi:[1,0]
	v_pk_add_f32 v[110:111], v[110:111], v[112:113]
	v_pk_add_f32 v[54:55], v[54:55], v[58:59]
	v_pk_add_f32 v[58:59], v[110:111], v[114:115]
	v_pk_add_f32 v[54:55], v[54:55], v[62:63]
	v_pk_add_f32 v[58:59], v[58:59], v[116:117]
	v_lshlrev_b32_e32 v62, 16, v200
	v_and_b32_e32 v63, 0xffff0000, v200
	v_pk_add_f32 v[54:55], v[54:55], v[66:67]
	v_lshlrev_b32_e32 v66, 16, v201
	v_and_b32_e32 v67, 0xffff0000, v201
	v_pk_fma_f32 v[58:59], v[84:85], v[58:59], v[62:63]
	v_pk_fma_f32 v[54:55], v[82:83], v[54:55], v[66:67]
	v_mov_b32_e32 v66, v69
	v_mov_b32_e32 v67, v59
	v_mov_b32_e32 v62, v68
	v_mov_b32_e32 v63, v58
	v_pk_mul_f32 v[66:67], v[66:67], v[66:67]
	v_add_f32_e32 v60, v60, v61
	v_pk_fma_f32 v[62:63], v[62:63], v[62:63], v[66:67]
	v_mov_b32_e32 v66, v64
	v_mov_b32_e32 v67, v54
	v_pk_fma_f32 v[62:63], v[66:67], v[66:67], v[62:63]
	v_mov_b32_e32 v66, v65
	v_mov_b32_e32 v67, v55
	v_pk_fma_f32 v[62:63], v[66:67], v[66:67], v[62:63]
	v_mbcnt_lo_u32_b32 v61, -1, 0
	v_mbcnt_hi_u32_b32 v61, -1, v61
	s_nop 0
	v_add_f32_e32 v60, v60, v62
	v_lshlrev_b32_e32 v61, 2, v61
	v_add_f32_e32 v60, v60, v63
	v_xor_b32_e32 v61, 0x80, v61
	ds_bpermute_b32 v61, v61, v60
	s_waitcnt lgkmcnt(0)
	v_add_f32_e32 v60, v60, v61
	v_mbcnt_lo_u32_b32 v61, -1, 0
	v_mbcnt_hi_u32_b32 v61, -1, v61
	s_nop 0
	v_lshlrev_b32_e32 v61, 2, v61
	v_xor_b32_e32 v61, 64, v61
	ds_bpermute_b32 v61, v61, v60
	s_waitcnt lgkmcnt(0)
	v_add_f32_e32 v60, v60, v61
	v_mbcnt_lo_u32_b32 v61, -1, 0
	v_mbcnt_hi_u32_b32 v61, -1, v61
	s_nop 0
	v_lshlrev_b32_e32 v61, 2, v61
	v_xor_b32_e32 v61, 32, v61
	ds_bpermute_b32 v61, v61, v60
	s_waitcnt lgkmcnt(0)
	v_add_f32_e32 v60, v60, v61
	v_mbcnt_lo_u32_b32 v61, -1, 0
	v_mbcnt_hi_u32_b32 v61, -1, v61
	s_nop 0
	v_lshlrev_b32_e32 v61, 2, v61
	v_xor_b32_e32 v61, 16, v61
	ds_bpermute_b32 v61, v61, v60
	s_waitcnt lgkmcnt(0)
	v_add_f32_e32 v60, v60, v61
	v_mbcnt_lo_u32_b32 v61, -1, 0
	v_mbcnt_hi_u32_b32 v61, -1, v61
	s_nop 0
	v_lshlrev_b32_e32 v61, 2, v61
	v_xor_b32_e32 v61, 8, v61
	ds_bpermute_b32 v61, v61, v60
	s_waitcnt lgkmcnt(0)
	v_add_f32_e32 v60, v60, v61
	v_mbcnt_lo_u32_b32 v61, -1, 0
	v_mbcnt_hi_u32_b32 v61, -1, v61
	s_nop 0
	v_lshlrev_b32_e32 v61, 2, v61
	v_xor_b32_e32 v61, 4, v61
	ds_bpermute_b32 v61, v61, v60
	s_waitcnt lgkmcnt(0)
	v_add_f32_e32 v60, v60, v61
	v_mov_b32_e32 v61, s18
	v_fmac_f32_e32 v61, 0x3a800000, v60
	v_cmp_gt_f32_e32 vcc, s80, v61
	v_mul_f32_e32 v60, 0x4b800000, v61
	s_nop 0
	v_cndmask_b32_e32 v60, v61, v60, vcc
	v_rsq_f32_e32 v60, v60
	s_nop 0
	v_mul_f32_e32 v61, 0x45800000, v60
	v_cndmask_b32_e32 v60, v60, v61, vcc
	s_and_b64 vcc, exec, s[6:7]
	s_cbranch_vccnz .LBB0_1514
; __device__ __forceinline__ unsigned cvt_pk_bf16(float lo, float hi) { const bf16x2_t r = __builtin_convertvector((f32x2_t){lo, hi}, bf16x2_t); return __builtin_bit_cast(unsigned, r); }
; __device__ __forceinline__ void combine_phase(LAS unsigned char* lds, const bf16_t* X, bf16_t* Xo, const unsigned char* __restrict__ YB, const float* __restrict__ mod_l, const int* __restrict__ cnt_l, ...
;     ...
;                 u32x4 xo0, xo1, h0, h1;
;                 xo0.x = cvt_pk_bf16(v[0][0], v[0][1]); xo0.y = cvt_pk_bf16(v[0][2], v[0][3]); xo0.z = cvt_pk_bf16(v[1][0], v[1][1]); xo0.w = cvt_pk_bf16(v[1][2], v[1][3]);
;                 xo1.x = cvt_pk_bf16(v[2][0], v[2][1]); xo1.y = cvt_pk_bf16(v[2][2], v[2][3]); xo1.z = cvt_pk_bf16(v[3][0], v[3][1]); xo1.w = cvt_pk_bf16(v[3][2], v[3][3]);
;                 *(u32x4*)(Xo + (size_t)t * D + k0) = xo0; *(u32x4*)(Xo + (size_t)t * D + k0 + 8) = xo1;
;                 f32x4 o[4];
; #pragma unroll
;                 for (int q = 0; q < 4; ++q) o[q] = v[q] * r * gn[q] + sh[q];
;                 h0.x = cvt_pk_bf16(o[0][0], o[0][1]); h0.y = cvt_pk_bf16(o[0][2], o[0][3]); h0.z = cvt_pk_bf16(o[1][0], o[1][1]); h0.w = cvt_pk_bf16(o[1][2], o[1][3]);
;                 h1.x = cvt_pk_bf16(o[2][0], o[2][1]); h1.y = cvt_pk_bf16(o[2][2], o[2][3]); h1.z = cvt_pk_bf16(o[3][0], o[3][1]); h1.w = cvt_pk_bf16(o[3][2], o[3][3]);
;                 *(u32x4*)(H1B + (size_t)t * D + k0) = h0; *(u32x4*)(H1B + (size_t)t * D + k0 + 8) = h1;
	v_lshlrev_b64 v[62:63], 1, v[100:101]
	v_cvt_pk_bf16_f32 v110, v104, v105
	v_cvt_pk_bf16_f32 v111, v102, v103
	v_cvt_pk_bf16_f32 v112, v56, v57
	v_cvt_pk_bf16_f32 v113, v52, v53
	v_lshl_add_u64 v[66:67], v[76:77], 0, v[62:63]
	v_cvt_pk_bf16_f32 v114, v68, v69
	v_cvt_pk_bf16_f32 v115, v64, v65
	v_cvt_pk_bf16_f32 v116, v58, v59
	v_cvt_pk_bf16_f32 v117, v54, v55
	global_store_dwordx4 v[66:67], v[110:113], off
	global_store_dwordx4 v[66:67], v[114:117], off offset:16
	v_pk_mul_f32 v[66:67], v[102:103], v[60:61] op_sel_hi:[1,0]
	v_pk_mul_f32 v[110:111], v[52:53], v[60:61] op_sel_hi:[1,0]
	v_pk_mul_f32 v[70:71], v[104:105], v[60:61] op_sel_hi:[1,0]
	v_pk_mul_f32 v[112:113], v[56:57], v[60:61] op_sel_hi:[1,0]
	v_pk_fma_f32 v[114:115], v[32:33], v[110:111], v[20:21]
	v_pk_mul_f32 v[110:111], v[64:65], v[60:61] op_sel_hi:[1,0]
	v_pk_fma_f32 v[66:67], v[28:29], v[66:67], v[24:25]
	v_pk_fma_f32 v[70:71], v[26:27], v[70:71], v[22:23]
	v_pk_fma_f32 v[112:113], v[30:31], v[112:113], v[18:19]
	v_pk_mul_f32 v[116:117], v[68:69], v[60:61] op_sel_hi:[1,0]
	v_pk_fma_f32 v[118:119], v[46:47], v[110:111], v[42:43]
	v_pk_mul_f32 v[110:111], v[54:55], v[60:61] op_sel_hi:[1,0]
	v_pk_mul_f32 v[120:121], v[58:59], v[60:61] op_sel_hi:[1,0]
	v_pk_fma_f32 v[116:117], v[44:45], v[116:117], v[40:41]
	v_pk_fma_f32 v[122:123], v[50:51], v[110:111], v[38:39]
	v_pk_fma_f32 v[120:121], v[48:49], v[120:121], v[36:37]
	v_cvt_pk_bf16_f32 v110, v70, v71
	v_cvt_pk_bf16_f32 v111, v66, v67
	v_cvt_pk_bf16_f32 v112, v112, v113
	v_cvt_pk_bf16_f32 v113, v114, v115
	v_lshl_add_u64 v[62:63], v[78:79], 0, v[62:63]
	v_cvt_pk_bf16_f32 v114, v116, v117
	v_cvt_pk_bf16_f32 v115, v118, v119
	v_cvt_pk_bf16_f32 v116, v120, v121
	v_cvt_pk_bf16_f32 v117, v122, v123
	global_store_dwordx4 v[62:63], v[110:113], off
	global_store_dwordx4 v[62:63], v[114:117], off offset:16
	s_cbranch_execnz .LBB0_1507
	s_branch .LBB0_1506
